# speedup vs baseline: 1.0028x; 1.0014x over previous
.LBB4_118:
	s_or_b64 exec, exec, s[0:1]
	s_waitcnt lgkmcnt(0)
	s_barrier
	s_waitcnt vmcnt(0)
	ds_read_b128 v[18:21], v75 offset:8192
	ds_read_b128 v[22:25], v74
	ds_read_b128 v[26:29], v75 offset:9216
	v_or_b32_e32 v30, s29, v98
	v_add_lshl_u32 v0, s27, v1, 9
	v_mov_b32_e32 v1, 0
	s_waitcnt lgkmcnt(1)
	v_mfma_f32_16x16x32_f16 v[2:5], v[18:21], v[22:25], v[2:5]
	ds_read_b128 v[18:21], v75 offset:10240
	s_waitcnt lgkmcnt(1)
	v_mfma_f32_16x16x32_f16 v[6:9], v[26:29], v[22:25], v[6:9]
	ds_read_b128 v[26:29], v75 offset:11264
	s_waitcnt lgkmcnt(1)
	v_mfma_f32_16x16x32_f16 v[10:13], v[18:21], v[22:25], v[10:13]
	v_lshl_add_u64 v[18:19], s[6:7], 0, v[0:1]
	v_lshlrev_b32_e32 v0, 2, v30
	v_lshl_add_u64 v[0:1], v[18:19], 0, v[0:1]
	v_lshl_add_u64 v[18:19], v[0:1], 0, v[40:41]
	global_store_dword v[18:19], v2, off sc1 nt
	v_lshl_add_u64 v[18:19], v[0:1], 0, v[42:43]
	global_store_dword v[18:19], v3, off sc1 nt
	v_lshl_add_u64 v[2:3], v[0:1], 0, v[44:45]
	global_store_dword v[2:3], v4, off sc1 nt
	v_lshl_add_u64 v[2:3], v[0:1], 0, v[46:47]
	global_store_dword v[2:3], v5, off sc1 nt
	v_lshl_add_u64 v[2:3], v[0:1], 0, v[48:49]
	global_store_dword v[2:3], v6, off sc1 nt
	v_lshl_add_u64 v[2:3], v[0:1], 0, v[50:51]
	global_store_dword v[2:3], v7, off sc1 nt
	v_lshl_add_u64 v[2:3], v[0:1], 0, v[52:53]
	global_store_dword v[2:3], v8, off sc1 nt
	v_lshl_add_u64 v[2:3], v[0:1], 0, v[54:55]
	global_store_dword v[2:3], v9, off sc1 nt
	v_lshl_add_u64 v[2:3], v[0:1], 0, v[56:57]
	s_waitcnt lgkmcnt(0)
	v_mfma_f32_16x16x32_f16 v[14:17], v[26:29], v[22:25], v[14:17]
	global_store_dword v[2:3], v10, off sc1 nt
	v_lshl_add_u64 v[2:3], v[0:1], 0, v[58:59]
	global_store_dword v[2:3], v11, off sc1 nt
	v_lshl_add_u64 v[2:3], v[0:1], 0, v[60:61]
	global_store_dword v[2:3], v12, off sc1 nt
	v_lshl_add_u64 v[2:3], v[0:1], 0, v[62:63]
	global_store_dword v[2:3], v13, off sc1 nt
	v_lshl_add_u64 v[2:3], v[0:1], 0, v[64:65]
	global_store_dword v[2:3], v14, off sc1 nt
	v_lshl_add_u64 v[2:3], v[0:1], 0, v[66:67]
	global_store_dword v[2:3], v15, off sc1 nt
	v_lshl_add_u64 v[2:3], v[0:1], 0, v[68:69]
	v_lshl_add_u64 v[0:1], v[0:1], 0, v[70:71]
	global_store_dword v[2:3], v16, off sc1 nt
	global_store_dword v[0:1], v17, off sc1 nt
	s_endpgm
